# moe_stagger: work groups of an XCD offset by s_sleep steps (8 groups x 1.5us) at MoE phase start so up-epilogue write-through bursts do not coincide
# speedup vs baseline: 1.0177x; 1.0011x over previous
.LBB0_1847:
	s_or_b64 exec, exec, s[0:1]
	v_readlane_b32 s0, v254, 4
	s_mov_b32 s2, 0
	s_mov_b32 s4, s0
	v_readlane_b32 s54, v254, 2
	v_readlane_b32 s0, v254, 3
	s_waitcnt lgkmcnt(0)
	s_barrier
	s_lshr_b32 s98, s4, 3
	s_and_b32 s98, s98, 7
	s_cmp_eq_u32 s98, 0
	s_cbranch_scc1 .Lstg_done
.Lstg_loop:
	s_sleep 56
	s_add_i32 s98, s98, -1
	s_cmp_lg_u32 s98, 0
	s_cbranch_scc1 .Lstg_loop
.Lstg_done:
	v_readlane_b32 s100, v254, 26
	v_and_b32_e32 v251, 63, v0
	s_nop 1
	v_lshl_add_u32 v251, v251, 2, s100
	ds_read_b32 v251, v251
	s_mov_b32 s0, 23
	s_ashr_i32 s1, s0, 31
	s_lshl_b64 s[0:1], s[0:1], 3
	s_add_u32 s0, s94, s0
	s_addc_u32 s1, s95, s1
	s_load_dwordx2 s[24:25], s[0:1], 0x0
	v_readlane_b32 s0, v254, 50
	v_mov_b32_e32 v5, v0
	s_ashr_i32 s5, s4, 31
	v_mov_b32_e32 v2, s0
	ds_read_b32 v2, v2
	s_mov_b32 s55, 0
	v_readfirstlane_b32 s26, v5
	s_mov_b32 s3, 8
	s_mov_b64 s[0:1], s[4:5]
	s_waitcnt lgkmcnt(0)
	v_readfirstlane_b32 s6, v2
	s_ashr_i32 s7, s6, 31
	s_lshl_b64 s[10:11], s[6:7], 3
	v_mov_b64_e32 v[6:7], s[10:11]
	v_cmp_ge_i64_e32 vcc, s[4:5], v[6:7]
	v_cmp_lt_i64_e64 s[8:9], s[4:5], v[6:7]
	s_cbranch_vccz .LBB0_1849
	s_sub_u32 s0, s4, s10
	s_subb_u32 s1, s5, s11
	s_lshl_b64 s[6:7], s[6:7], 2
	v_mov_b64_e32 v[6:7], s[6:7]
	v_cmp_lt_i64_e64 s[8:9], s[0:1], v[6:7]
	s_mov_b32 s3, 4
	s_mov_b32 s55, 1
